# expert-down piece loop: removed a redundant LDS drain in front of the first MFMA of every second piece (it waited for the next piece's fragment prefetch)
# baseline (speedup 1.0000x reference)
.LBB0_789:
	s_add_i32 s19, s6, 1
	s_lshl_b32 s4, s19, 14
	s_and_b32 s4, s4, 0x1c000
	v_add_u32_e32 v100, s4, v206
	ds_read_b128 v[120:123], v100
	ds_read_b128 v[124:127], v100 offset:1024
	ds_read_b128 v[112:115], v100 offset:2048
	ds_read_b128 v[116:119], v100 offset:3072
	ds_read_b128 v[104:107], v100 offset:8192
	ds_read_b128 v[108:111], v100 offset:9216
	ds_read_b128 v[96:99], v100 offset:10240
	ds_read_b128 v[100:103], v100 offset:11264
	v_med3_f32 v210, v132, s7, v209
	v_med3_f32 v160, v133, s7, v209
	v_cvt_pk_fp8_f32 v210, v210, v160
	v_med3_f32 v160, v134, s7, v209
	v_med3_f32 v161, v135, s7, v209
	v_cvt_pk_fp8_f32 v210, v160, v161 op_sel:[0,0,1]
	v_mfma_f32_16x16x128_f8f6f4 v[160:163], v[0:7], v[64:71], 0
	v_mfma_f32_16x16x128_f8f6f4 v[164:167], v[8:15], v[64:71], 0
	v_med3_f32 v211, v128, s7, v209
	v_med3_f32 v168, v129, s7, v209
	v_cvt_pk_fp8_f32 v211, v211, v168
	v_med3_f32 v168, v130, s7, v209
	v_med3_f32 v169, v131, s7, v209
	v_cvt_pk_fp8_f32 v211, v168, v169 op_sel:[0,0,1]
	v_mfma_f32_16x16x128_f8f6f4 v[168:171], v[16:23], v[64:71], 0
	v_mfma_f32_16x16x128_f8f6f4 v[172:175], v[24:31], v[64:71], 0
	s_lshl_b32 s22, s6, 6
	s_add_i32 s4, s22, 0x3c0
	s_and_b32 s4, s4, 0x3c0
	v_lshl_add_u32 v176, s4, 2, v208
	ds_read2_b32 v[176:177], v176 offset1:16
	v_mov_b32_e32 v219, v197
	s_waitcnt lgkmcnt(0)
	v_mov_b32_e32 v196, v176
	v_mov_b32_e32 v218, v177
	v_med3_f32 v212, v140, s7, v209
	v_med3_f32 v176, v141, s7, v209
	v_cvt_pk_fp8_f32 v212, v212, v176
	v_med3_f32 v176, v142, s7, v209
	v_med3_f32 v177, v143, s7, v209
	v_cvt_pk_fp8_f32 v212, v176, v177 op_sel:[0,0,1]
	v_mfma_f32_16x16x128_f8f6f4 v[176:179], v[0:7], v[72:79], 0
	v_mfma_f32_16x16x128_f8f6f4 v[180:183], v[8:15], v[72:79], 0
	v_med3_f32 v213, v136, s7, v209
	v_med3_f32 v184, v137, s7, v209
	v_cvt_pk_fp8_f32 v213, v213, v184
	v_med3_f32 v184, v138, s7, v209
	v_med3_f32 v185, v139, s7, v209
	v_cvt_pk_fp8_f32 v213, v184, v185 op_sel:[0,0,1]
	v_mfma_f32_16x16x128_f8f6f4 v[184:187], v[16:23], v[72:79], 0
	v_mfma_f32_16x16x128_f8f6f4 v[188:191], v[24:31], v[72:79], 0
	v_lshlrev_b64 v[216:217], 10, v[196:197]
	v_med3_f32 v214, v148, s7, v209
	v_med3_f32 v196, v149, s7, v209
	v_cvt_pk_fp8_f32 v214, v214, v196
	v_lshl_add_u64 v[216:217], v[198:199], 0, v[216:217]
	v_med3_f32 v196, v150, s7, v209
	v_med3_f32 v215, v151, s7, v209
	v_cvt_pk_fp8_f32 v214, v196, v215 op_sel:[0,0,1]
	global_store_dwordx4 v[216:217], v[210:213], off
	v_mfma_f32_16x16x128_f8f6f4 v[160:163], v[32:39], v[80:87], v[160:163]
	v_mfma_f32_16x16x128_f8f6f4 v[164:167], v[40:47], v[80:87], v[164:167]
	v_med3_f32 v215, v144, s7, v209
	v_med3_f32 v196, v145, s7, v209
	v_cvt_pk_fp8_f32 v215, v215, v196
	v_med3_f32 v196, v146, s7, v209
	v_med3_f32 v210, v147, s7, v209
	v_mfma_f32_16x16x128_f8f6f4 v[168:171], v[48:55], v[80:87], v[168:171]
	v_cvt_pk_fp8_f32 v215, v196, v210 op_sel:[0,0,1]
	v_mfma_f32_16x16x128_f8f6f4 v[172:175], v[56:63], v[80:87], v[172:175]
	v_med3_f32 v216, v156, s7, v209
	v_med3_f32 v196, v157, s7, v209
	v_cvt_pk_fp8_f32 v216, v216, v196
	v_med3_f32 v196, v158, s7, v209
	v_med3_f32 v210, v159, s7, v209
	v_mfma_f32_16x16x128_f8f6f4 v[176:179], v[32:39], v[88:95], v[176:179]
	v_cvt_pk_fp8_f32 v216, v196, v210 op_sel:[0,0,1]
	v_mfma_f32_16x16x128_f8f6f4 v[180:183], v[40:47], v[88:95], v[180:183]
	v_med3_f32 v217, v152, s7, v209
	v_med3_f32 v196, v153, s7, v209
	v_cvt_pk_fp8_f32 v217, v217, v196
	v_med3_f32 v196, v154, s7, v209
	v_med3_f32 v210, v155, s7, v209
	v_mfma_f32_16x16x128_f8f6f4 v[184:187], v[48:55], v[88:95], v[184:187]
	v_cvt_pk_fp8_f32 v217, v196, v210 op_sel:[0,0,1]
	v_mfma_f32_16x16x128_f8f6f4 v[188:191], v[56:63], v[88:95], v[188:191]
	v_lshlrev_b64 v[210:211], 10, v[218:219]
	v_lshl_add_u64 v[210:211], v[198:199], 0, v[210:211]
	s_cmp_ge_i32 s19, s25
	global_store_dwordx4 v[210:211], v[214:217], off
	s_cbranch_scc1 .LBB0_774
	s_and_b32 s4, s19, 3
	s_cmp_eq_u32 s4, 0
	s_cbranch_scc1 .LBB0_792
	s_add_i32 s23, s19, s10
	s_cbranch_execz .LBB0_793
	s_branch .LBB0_800
